# combo11 + norm2 pass-1 loads quad-coalesced (lane quad = 64 contiguous bytes of a row), quad reduction + ds_bpermute back to the fragment layout
# speedup vs baseline: 1.0134x; 1.0014x over previous
.LBB0_881:
	s_or_b64 exec, exec, s[24:25]
	v_ashrrev_i32_e32 v113, 31, v112
	v_lshlrev_b64 v[26:27], 11, v[112:113]
	v_lshl_add_u64 v[0:1], v[92:93], 0, v[26:27]
	v_mbcnt_lo_u32_b32 v8, -1, 0
	v_mbcnt_hi_u32_b32 v8, -1, v8
	v_lshrrev_b32_e32 v9, 2, v8
	v_and_b32_e32 v12, 15, v8
	v_sub_u32_e32 v9, v9, v12
	v_and_b32_e32 v10, 3, v8
	v_lshrrev_b32_e32 v11, 4, v8
	v_sub_u32_e32 v10, v10, v11
	v_lshlrev_b32_e32 v9, 11, v9
	v_lshl_add_u32 v10, v10, 4, v9
	v_ashrrev_i32_e32 v11, 31, v10
	v_lshlrev_b32_e32 v172, 4, v12
	v_lshl_add_u64 v[0:1], v[0:1], 0, v[10:11]
	v_mov_b32_e32 v7, 0
	s_mov_b64 s[24:25], 0
	v_mov_b32_e32 v6, 0
	s_waitcnt lgkmcnt(0)
	s_barrier
.LBB0_882:
	v_lshl_add_u64 v[4:5], v[0:1], 0, s[24:25]
	v_add_co_u32_e32 v2, vcc, 0x34000000, v4
	s_add_u32 s24, s24, 0x200
	s_nop 0
	v_addc_co_u32_e32 v3, vcc, 0, v5, vcc
	v_add_co_u32_e32 v4, vcc, 0x34008000, v4
	s_nop 0
	s_nop 0
	v_addc_co_u32_e32 v5, vcc, 0, v5, vcc
	s_addc_u32 s25, s25, 0
	global_load_dwordx4 v[186:189], v[2:3], off
	global_load_dwordx4 v[190:193], v[4:5], off
	global_load_dwordx4 v[194:197], v[2:3], off offset:64
	global_load_dwordx4 v[198:201], v[4:5], off offset:64
	global_load_dwordx4 v[202:205], v[2:3], off offset:128
	global_load_dwordx4 v[206:209], v[4:5], off offset:128
	global_load_dwordx4 v[210:213], v[2:3], off offset:192
	global_load_dwordx4 v[214:217], v[4:5], off offset:192
	global_load_dwordx4 v[228:231], v[2:3], off offset:256
	global_load_dwordx4 v[232:235], v[4:5], off offset:256
	global_load_dwordx4 v[236:239], v[2:3], off offset:320
	global_load_dwordx4 v[244:247], v[4:5], off offset:320
	global_load_dwordx4 v[248:251], v[2:3], off offset:384
	global_load_dwordx4 v[160:163], v[4:5], off offset:384
	global_load_dwordx4 v[164:167], v[2:3], off offset:448
	global_load_dwordx4 v[168:171], v[4:5], off offset:448
	s_cmpk_eq_i32 s24, 0x800
	s_waitcnt vmcnt(14)
	v_dot2c_f32_bf16_e32 v7, v186, v186
	v_dot2c_f32_bf16_e32 v7, v187, v187
	v_dot2c_f32_bf16_e32 v7, v188, v188
	v_dot2c_f32_bf16_e32 v7, v189, v189
	v_dot2c_f32_bf16_e32 v6, v190, v190
	v_dot2c_f32_bf16_e32 v6, v191, v191
	v_dot2c_f32_bf16_e32 v6, v192, v192
	v_dot2c_f32_bf16_e32 v6, v193, v193
	s_waitcnt vmcnt(12)
	v_dot2c_f32_bf16_e32 v7, v194, v194
	v_dot2c_f32_bf16_e32 v7, v195, v195
	v_dot2c_f32_bf16_e32 v7, v196, v196
	v_dot2c_f32_bf16_e32 v7, v197, v197
	v_dot2c_f32_bf16_e32 v6, v198, v198
	v_dot2c_f32_bf16_e32 v6, v199, v199
	v_dot2c_f32_bf16_e32 v6, v200, v200
	v_dot2c_f32_bf16_e32 v6, v201, v201
	s_waitcnt vmcnt(10)
	v_dot2c_f32_bf16_e32 v7, v202, v202
	v_dot2c_f32_bf16_e32 v7, v203, v203
	v_dot2c_f32_bf16_e32 v7, v204, v204
	v_dot2c_f32_bf16_e32 v7, v205, v205
	v_dot2c_f32_bf16_e32 v6, v206, v206
	v_dot2c_f32_bf16_e32 v6, v207, v207
	v_dot2c_f32_bf16_e32 v6, v208, v208
	v_dot2c_f32_bf16_e32 v6, v209, v209
	s_waitcnt vmcnt(8)
	v_dot2c_f32_bf16_e32 v7, v210, v210
	v_dot2c_f32_bf16_e32 v7, v211, v211
	v_dot2c_f32_bf16_e32 v7, v212, v212
	v_dot2c_f32_bf16_e32 v7, v213, v213
	v_dot2c_f32_bf16_e32 v6, v214, v214
	v_dot2c_f32_bf16_e32 v6, v215, v215
	v_dot2c_f32_bf16_e32 v6, v216, v216
	v_dot2c_f32_bf16_e32 v6, v217, v217
	s_waitcnt vmcnt(6)
	v_dot2c_f32_bf16_e32 v7, v228, v228
	v_dot2c_f32_bf16_e32 v7, v229, v229
	v_dot2c_f32_bf16_e32 v7, v230, v230
	v_dot2c_f32_bf16_e32 v7, v231, v231
	v_dot2c_f32_bf16_e32 v6, v232, v232
	v_dot2c_f32_bf16_e32 v6, v233, v233
	v_dot2c_f32_bf16_e32 v6, v234, v234
	v_dot2c_f32_bf16_e32 v6, v235, v235
	s_waitcnt vmcnt(4)
	v_dot2c_f32_bf16_e32 v7, v236, v236
	v_dot2c_f32_bf16_e32 v7, v237, v237
	v_dot2c_f32_bf16_e32 v7, v238, v238
	v_dot2c_f32_bf16_e32 v7, v239, v239
	v_dot2c_f32_bf16_e32 v6, v244, v244
	v_dot2c_f32_bf16_e32 v6, v245, v245
	v_dot2c_f32_bf16_e32 v6, v246, v246
	v_dot2c_f32_bf16_e32 v6, v247, v247
	s_waitcnt vmcnt(2)
	v_dot2c_f32_bf16_e32 v7, v248, v248
	v_dot2c_f32_bf16_e32 v7, v249, v249
	v_dot2c_f32_bf16_e32 v7, v250, v250
	v_dot2c_f32_bf16_e32 v7, v251, v251
	v_dot2c_f32_bf16_e32 v6, v160, v160
	v_dot2c_f32_bf16_e32 v6, v161, v161
	v_dot2c_f32_bf16_e32 v6, v162, v162
	v_dot2c_f32_bf16_e32 v6, v163, v163
	s_waitcnt vmcnt(0)
	v_dot2c_f32_bf16_e32 v7, v164, v164
	v_dot2c_f32_bf16_e32 v7, v165, v165
	v_dot2c_f32_bf16_e32 v7, v166, v166
	v_dot2c_f32_bf16_e32 v7, v167, v167
	v_dot2c_f32_bf16_e32 v6, v168, v168
	v_dot2c_f32_bf16_e32 v6, v169, v169
	v_dot2c_f32_bf16_e32 v6, v170, v170
	v_dot2c_f32_bf16_e32 v6, v171, v171
	s_cbranch_scc0 .LBB0_882
	s_lshl_b32 s50, s0, 8
	s_add_i32 s50, s50, s38
	v_or_b32_e32 v0, s50, v136
	v_ashrrev_i32_e32 v1, 31, v0
	v_lshlrev_b64 v[0:1], 11, v[0:1]
	v_lshl_add_u64 v[120:121], v[94:95], 0, v[0:1]
	s_nop 1
	v_add_f32_dpp v25, v7, v7 quad_perm:[1,0,3,2] row_mask:0xf bank_mask:0xf
	v_add_f32_dpp v31, v6, v6 quad_perm:[1,0,3,2] row_mask:0xf bank_mask:0xf
	s_nop 1
	v_add_f32_dpp v25, v25, v25 quad_perm:[2,3,0,1] row_mask:0xf bank_mask:0xf
	v_add_f32_dpp v31, v31, v31 quad_perm:[2,3,0,1] row_mask:0xf bank_mask:0xf
	s_nop 1
	ds_bpermute_b32 v25, v172, v25
	ds_bpermute_b32 v31, v172, v31
	v_mov_b32_e32 v29, 0
	v_mov_b32_e32 v30, 0
	s_waitcnt lgkmcnt(0)
	v_mov_b32_e32 v36, v185
	v_mov_b32_e32 v28, v185
	v_add_co_u32_e32 v0, vcc, 0x8000, v120
	v_mov_b32_e32 v32, v185
	v_mov_b32_e32 v24, v185
	v_mov_b32_e32 v113, 0x43e00000
	v_addc_co_u32_e32 v1, vcc, 0, v121, vcc
	global_load_dwordx4 v[20:23], v[120:121], off
	global_load_dwordx4 v[16:19], v[0:1], off
	s_nop 0
	global_load_dwordx4 v[0:3], v[102:103], off
	global_load_dwordx4 v[4:7], v[104:105], off
	global_load_dwordx4 v[8:11], v[106:107], off
	global_load_dwordx4 v[12:15], v[108:109], off
	v_add_f32_e32 v25, v25, v29
	v_add_f32_e32 v29, v31, v30
	v_fmamk_f32 v25, v25, 0x3a800000, v252
	v_fmamk_f32 v29, v29, 0x3a800000, v252
	v_rsq_f32_e32 v126, v29
	v_rsq_f32_e32 v128, v25
	v_ashrrev_i32_e32 v115, 31, v114
	s_mov_b64 s[24:25], 0x8000
	v_lshlrev_b64 v[124:125], 10, v[114:115]
	v_lshl_add_u64 v[122:123], v[120:121], 0, s[24:25]
	v_or_b32_e32 v124, v96, v124
	v_lshl_add_u64 v[130:131], v[90:91], 0, v[26:27]
	v_mov_b32_e32 v127, v126
	v_mov_b32_e32 v129, v128
	s_mov_b32 s24, 64
	v_mov_b64_e32 v[132:133], v[116:117]
	v_mov_b32_e32 v115, v144
	v_mov_b32_e32 v37, v36
	v_mov_b32_e32 v38, v36
	v_mov_b32_e32 v39, v36
	v_mov_b32_e32 v29, v28
	v_mov_b32_e32 v30, v28
	v_mov_b32_e32 v31, v28
	v_mov_b32_e32 v33, v32
	v_mov_b32_e32 v34, v32
	v_mov_b32_e32 v35, v32
	v_mov_b32_e32 v25, v24
	v_mov_b32_e32 v26, v24
	v_mov_b32_e32 v27, v24
